# speedup vs baseline: 1.0072x; 1.0072x over previous
.Lk2_s00:
	s_cmp_eq_u32 s17, 16
	s_cbranch_scc1 .Lk2_b00
	s_waitcnt vmcnt(12)
	s_barrier
